# speedup vs baseline: 1.0174x; 1.0174x over previous
.LBB0_120:
	s_cmpk_gt_u32 s33, 0x7f
	s_waitcnt lgkmcnt(0)
	s_cbranch_scc1 .Lmlp_others
	v_mbcnt_lo_u32_b32 v92, -1, 0
	v_mbcnt_hi_u32_b32 v92, -1, v92
	v_mov_b32_e32 v1, 0x15300
	v_ashrrev_i32_e32 v0, 5, v92
	s_waitcnt vmcnt(0)
	v_and_or_b32 v37, v92, 31, s31
	v_lshlrev_b32_e32 v38, 4, v0
	v_lshl_add_u32 v1, v37, 2, v1
	v_add_u32_e32 v93, 0x14c00, v38
	ds_read_b32 v36, v1
	ds_read_b128 v[0:3], v93
	ds_read_b128 v[4:7], v93 offset:32
	ds_read_b128 v[8:11], v93 offset:64
	v_add_u32_e32 v39, v93, v38
	ds_read_b128 v[24:27], v39 offset:1280
	ds_read_b128 v[28:31], v39 offset:1024
	ds_read_b128 v[12:15], v93 offset:96
	ds_read_b128 v[16:19], v93 offset:128
	ds_read_b128 v[20:23], v39 offset:1040
	ds_read_b128 v[32:35], v39 offset:1232
	ds_read_b128 v[80:83], v93 offset:992
	s_waitcnt lgkmcnt(5)
	v_fma_f32 v24, v36, v28, v24
	v_max_f32_e32 v44, 0, v24
	v_fma_f32 v24, v36, v29, v25
	ds_read_b128 v[40:43], v39 offset:1296
	v_max_f32_e32 v45, 0, v24
	v_fma_f32 v24, v36, v30, v26
	v_fmac_f32_e32 v27, v36, v31
	v_max_f32_e32 v46, 0, v24
	v_max_f32_e32 v47, 0, v27
	ds_read_b128 v[24:27], v39 offset:1088
	ds_read_b128 v[28:31], v39 offset:1344
	s_waitcnt lgkmcnt(2)
	v_fma_f32 v20, v36, v20, v40
	v_fma_f32 v21, v36, v21, v41
	v_max_f32_e32 v20, 0, v20
	v_max_f32_e32 v21, 0, v21
	v_fma_f32 v22, v36, v22, v42
	v_cvt_pk_f16_f32 v42, v20, v21
	s_waitcnt lgkmcnt(0)
	v_fma_f32 v20, v36, v24, v28
	v_fmac_f32_e32 v43, v36, v23
	v_max_f32_e32 v48, 0, v20
	v_fma_f32 v20, v36, v25, v29
	v_max_f32_e32 v22, 0, v22
	v_max_f32_e32 v23, 0, v43
	v_max_f32_e32 v49, 0, v20
	v_fma_f32 v20, v36, v26, v30
	v_cvt_pk_f16_f32 v43, v22, v23
	v_cvt_pk_f16_f32 v41, v46, v47
	v_cvt_pk_f16_f32 v40, v44, v45
	v_max_f32_e32 v50, 0, v20
	ds_read_b128 v[20:23], v39 offset:1104
	ds_read_b128 v[44:47], v39 offset:1360
	v_fmac_f32_e32 v31, v36, v27
	v_max_f32_e32 v51, 0, v31
	ds_read_b128 v[24:27], v39 offset:1152
	ds_read_b128 v[28:31], v39 offset:1408
	v_lshlrev_b32_e32 v94, 4, v92
	s_waitcnt lgkmcnt(2)
	v_fma_f32 v20, v36, v20, v44
	v_fma_f32 v21, v36, v21, v45
	v_max_f32_e32 v20, 0, v20
	v_max_f32_e32 v21, 0, v21
	v_fma_f32 v22, v36, v22, v46
	v_cvt_pk_f16_f32 v46, v20, v21
	s_waitcnt lgkmcnt(0)
	v_fma_f32 v20, v36, v24, v28
	v_fmac_f32_e32 v47, v36, v23
	v_max_f32_e32 v52, 0, v20
	v_fma_f32 v20, v36, v25, v29
	v_max_f32_e32 v22, 0, v22
	v_max_f32_e32 v23, 0, v47
	v_max_f32_e32 v53, 0, v20
	v_fma_f32 v20, v36, v26, v30
	v_cvt_pk_f16_f32 v47, v22, v23
	v_cvt_pk_f16_f32 v45, v50, v51
	v_cvt_pk_f16_f32 v44, v48, v49
	v_max_f32_e32 v54, 0, v20
	ds_read_b128 v[20:23], v39 offset:1168
	ds_read_b128 v[48:51], v39 offset:1424
	v_fmac_f32_e32 v31, v36, v27
	v_max_f32_e32 v55, 0, v31
	ds_read_b128 v[24:27], v39 offset:1216
	ds_read_b128 v[28:31], v39 offset:1472
	v_cvt_pk_f16_f32 v84, v52, v53
	s_waitcnt lgkmcnt(2)
	v_fma_f32 v20, v36, v20, v48
	v_fma_f32 v21, v36, v21, v49
	v_fma_f32 v22, v36, v22, v50
	v_fmac_f32_e32 v51, v36, v23
	v_max_f32_e32 v20, 0, v20
	v_max_f32_e32 v21, 0, v21
	v_max_f32_e32 v22, 0, v22
	v_max_f32_e32 v23, 0, v51
	v_cvt_pk_f16_f32 v87, v22, v23
	v_cvt_pk_f16_f32 v86, v20, v21
	ds_read_b128 v[20:23], v94
	ds_read_b128 v[48:51], v94 offset:1024
	s_waitcnt lgkmcnt(1)
	v_mfma_f32_32x32x16_f16 v[0:15], v[20:23], v[40:43], v[0:15]
	v_fma_f32 v24, v36, v24, v28
	v_max_f32_e32 v52, 0, v24
	v_fma_f32 v24, v36, v25, v29
	v_max_f32_e32 v53, 0, v24
	v_fma_f32 v24, v36, v26, v30
	v_cvt_pk_f16_f32 v85, v54, v55
	v_max_f32_e32 v54, 0, v24
	v_lshlrev_b32_e32 v24, 5, v37
	s_mov_b32 s0, 0x13400
	v_fmac_f32_e32 v31, v36, v27
	v_add3_u32 v28, v24, v38, s0
	ds_read_b128 v[24:27], v94 offset:2048
	s_waitcnt lgkmcnt(1)
	v_mfma_f32_32x32x16_f16 v[0:15], v[48:51], v[44:47], v[0:15]
	v_max_f32_e32 v55, 0, v31
	ds_read_b128 v[20:23], v39 offset:1488
	s_barrier
	ds_read_b128 v[88:91], v28
	ds_read_b128 v[28:31], v94 offset:3072
	v_cvt_pk_f16_f32 v37, v54, v55
	v_cmp_gt_u32_e32 vcc, 32, v92
	s_waitcnt lgkmcnt(2)
	v_fma_f32 v20, v36, v32, v20
	v_mfma_f32_32x32x16_f16 v[0:15], v[24:27], v[84:87], v[0:15]
	v_fma_f32 v21, v36, v33, v21
	v_fma_f32 v22, v36, v34, v22
	v_fmac_f32_e32 v23, v36, v35
	v_max_f32_e32 v20, 0, v20
	v_max_f32_e32 v21, 0, v21
	v_max_f32_e32 v22, 0, v22
	v_max_f32_e32 v23, 0, v23
	v_cvt_pk_f16_f32 v39, v22, v23
	v_cvt_pk_f16_f32 v38, v20, v21
	v_cvt_pk_f16_f32 v36, v52, v53
	ds_read_b128 v[20:23], v94 offset:4096
	ds_read_b128 v[32:35], v94 offset:5120
	s_waitcnt lgkmcnt(2)
	v_mfma_f32_32x32x16_f16 v[0:15], v[28:31], v[36:39], v[0:15]
	s_waitcnt lgkmcnt(1)
	v_mfma_f32_32x32x16_f16 v[0:15], v[20:23], v[88:91], v[0:15]
	ds_read_b128 v[20:23], v93 offset:160
	ds_read_b128 v[24:27], v93 offset:192
	ds_read_b128 v[28:31], v93 offset:224
	ds_read_b128 v[64:67], v93 offset:256
	s_waitcnt lgkmcnt(1)
	v_mfma_f32_32x32x16_f16 v[16:31], v[32:35], v[40:43], v[16:31]
	ds_read_b128 v[32:35], v94 offset:6144
	ds_read_b128 v[48:51], v94 offset:7168
	s_nop 3
	v_max_f32_e32 v4, v4, v4
	v_max_f32_e32 v5, v5, v5
	v_max_f32_e32 v6, v6, v6
	v_max_f32_e32 v7, v7, v7
	v_max_f32_e32 v4, 0, v4
	v_max_f32_e32 v5, 0, v5
	s_waitcnt lgkmcnt(1)
	v_mfma_f32_32x32x16_f16 v[16:31], v[32:35], v[44:47], v[16:31]
	v_max_f32_e32 v6, 0, v6
	v_max_f32_e32 v7, 0, v7
	v_max_f32_e32 v2, v2, v2
	v_max_f32_e32 v3, v3, v3
	v_max_f32_e32 v2, 0, v2
	v_max_f32_e32 v3, 0, v3
	v_max_f32_e32 v0, v0, v0
	s_waitcnt lgkmcnt(0)
	v_mfma_f32_32x32x16_f16 v[16:31], v[48:51], v[84:87], v[16:31]
	ds_read_b128 v[32:35], v94 offset:8192
	ds_read_b128 v[48:51], v94 offset:9216
	v_max_f32_e32 v1, v1, v1
	v_max_f32_e32 v0, 0, v0
	v_max_f32_e32 v1, 0, v1
	s_waitcnt lgkmcnt(1)
	v_mfma_f32_32x32x16_f16 v[16:31], v[32:35], v[36:39], v[16:31]
	ds_read_b128 v[32:35], v94 offset:10240
	s_waitcnt lgkmcnt(1)
	v_mfma_f32_32x32x16_f16 v[16:31], v[48:51], v[88:91], v[16:31]
	ds_read_b128 v[68:71], v93 offset:288
	ds_read_b128 v[72:75], v93 offset:320
	ds_read_b128 v[76:79], v93 offset:352
	ds_read_b128 v[48:51], v93 offset:384
	ds_read_b128 v[52:55], v94 offset:11264
	s_waitcnt lgkmcnt(2)
	v_mfma_f32_32x32x16_f16 v[64:79], v[32:35], v[40:43], v[64:79]
	s_waitcnt lgkmcnt(0)
	v_mfma_f32_32x32x16_f16 v[64:79], v[52:55], v[44:47], v[64:79]
	ds_read_b128 v[32:35], v94 offset:12288
	ds_read_b128 v[52:55], v94 offset:13312
	s_waitcnt lgkmcnt(1)
	v_mfma_f32_32x32x16_f16 v[64:79], v[32:35], v[84:87], v[64:79]
	ds_read_b128 v[32:35], v94 offset:14336
	ds_read_b128 v[96:99], v94 offset:15360
	s_waitcnt lgkmcnt(2)
	v_mfma_f32_32x32x16_f16 v[64:79], v[52:55], v[36:39], v[64:79]
	s_waitcnt lgkmcnt(1)
	v_mfma_f32_32x32x16_f16 v[64:79], v[32:35], v[88:91], v[64:79]
	ds_read_b128 v[52:55], v93 offset:416
	ds_read_b128 v[56:59], v93 offset:448
	ds_read_b128 v[60:63], v93 offset:480
	ds_read_b128 v[32:35], v93 offset:512
	s_waitcnt lgkmcnt(1)
	v_mfma_f32_32x32x16_f16 v[48:63], v[96:99], v[40:43], v[48:63]
	ds_read_b128 v[40:43], v94 offset:16384
	ds_read_b128 v[96:99], v94 offset:17408
	s_waitcnt lgkmcnt(1)
	v_mfma_f32_32x32x16_f16 v[48:63], v[40:43], v[44:47], v[48:63]
	ds_read_b128 v[40:43], v94 offset:18432
	ds_read_b128 v[44:47], v94 offset:19456
	s_waitcnt lgkmcnt(2)
	v_mfma_f32_32x32x16_f16 v[48:63], v[96:99], v[84:87], v[48:63]
	v_cvt_pk_f16_f32 v87, v6, v7
	v_cvt_pk_f16_f32 v86, v4, v5
	v_max_f32_e32 v4, v12, v12
	v_max_f32_e32 v5, v13, v13
	v_max_f32_e32 v6, v14, v14
	v_max_f32_e32 v7, v15, v15
	v_max_f32_e32 v4, 0, v4
	s_waitcnt lgkmcnt(1)
	v_mfma_f32_32x32x16_f16 v[48:63], v[40:43], v[36:39], v[48:63]
	v_max_f32_e32 v5, 0, v5
	v_max_f32_e32 v6, 0, v6
	v_max_f32_e32 v7, 0, v7
	v_cvt_pk_f16_f32 v85, v2, v3
	v_max_f32_e32 v2, v10, v10
	v_max_f32_e32 v3, v11, v11
	v_max_f32_e32 v2, 0, v2
	s_waitcnt lgkmcnt(0)
	v_mfma_f32_32x32x16_f16 v[48:63], v[44:47], v[88:91], v[48:63]
	v_cvt_pk_f16_f32 v91, v6, v7
	v_cvt_pk_f16_f32 v90, v4, v5
	v_max_f32_e32 v4, v20, v20
	v_max_f32_e32 v5, v21, v21
	v_max_f32_e32 v6, v22, v22
	v_max_f32_e32 v7, v23, v23
	v_max_f32_e32 v3, 0, v3
	v_max_f32_e32 v4, 0, v4
	v_max_f32_e32 v5, 0, v5
	v_max_f32_e32 v6, 0, v6
	v_max_f32_e32 v7, 0, v7
	v_cvt_pk_f16_f32 v89, v2, v3
	v_max_f32_e32 v2, v18, v18
	v_max_f32_e32 v3, v19, v19
	v_cvt_pk_f16_f32 v19, v6, v7
	v_cvt_pk_f16_f32 v18, v4, v5
	v_max_f32_e32 v4, v28, v28
	v_max_f32_e32 v5, v29, v29
	v_max_f32_e32 v6, v30, v30
	v_max_f32_e32 v7, v31, v31
	v_max_f32_e32 v4, 0, v4
	v_max_f32_e32 v5, 0, v5
	v_max_f32_e32 v6, 0, v6
	v_max_f32_e32 v7, 0, v7
	v_cvt_pk_f16_f32 v84, v0, v1
	v_max_f32_e32 v0, v8, v8
	v_max_f32_e32 v1, v9, v9
	v_cvt_pk_f16_f32 v23, v6, v7
	v_cvt_pk_f16_f32 v22, v4, v5
	v_max_f32_e32 v4, v68, v68
	v_max_f32_e32 v5, v69, v69
	v_max_f32_e32 v6, v70, v70
	v_max_f32_e32 v7, v71, v71
	v_max_f32_e32 v0, 0, v0
	v_max_f32_e32 v1, 0, v1
	v_max_f32_e32 v2, 0, v2
	v_max_f32_e32 v3, 0, v3
	v_max_f32_e32 v4, 0, v4
	v_max_f32_e32 v5, 0, v5
	v_max_f32_e32 v6, 0, v6
	v_max_f32_e32 v7, 0, v7
	v_cvt_pk_f16_f32 v88, v0, v1
	v_max_f32_e32 v0, v16, v16
	v_max_f32_e32 v1, v17, v17
	v_cvt_pk_f16_f32 v17, v2, v3
	v_max_f32_e32 v2, v26, v26
	v_max_f32_e32 v3, v27, v27
	v_cvt_pk_f16_f32 v27, v6, v7
	v_cvt_pk_f16_f32 v26, v4, v5
	ds_read_b128 v[4:7], v94 offset:20480
	v_max_f32_e32 v0, 0, v0
	v_max_f32_e32 v1, 0, v1
	v_cvt_pk_f16_f32 v16, v0, v1
	v_max_f32_e32 v0, v24, v24
	v_max_f32_e32 v1, v25, v25
	v_max_f32_e32 v0, 0, v0
	v_max_f32_e32 v1, 0, v1
	v_cvt_pk_f16_f32 v20, v0, v1
	v_max_f32_e32 v0, v64, v64
	v_max_f32_e32 v1, v65, v65
	ds_read_b128 v[36:39], v93 offset:544
	ds_read_b128 v[40:43], v93 offset:576
	ds_read_b128 v[44:47], v93 offset:608
	v_max_f32_e32 v0, 0, v0
	v_max_f32_e32 v1, 0, v1
	v_cvt_pk_f16_f32 v24, v0, v1
	v_max_f32_e32 v0, v72, v72
	v_max_f32_e32 v2, 0, v2
	v_max_f32_e32 v3, 0, v3
	v_max_f32_e32 v12, 0, v0
	v_max_f32_e32 v0, v73, v73
	v_cvt_pk_f16_f32 v21, v2, v3
	v_max_f32_e32 v2, v66, v66
	v_max_f32_e32 v3, v67, v67
	v_max_f32_e32 v13, 0, v0
	v_max_f32_e32 v0, v74, v74
	v_max_f32_e32 v2, 0, v2
	v_max_f32_e32 v3, 0, v3
	v_max_f32_e32 v14, 0, v0
	v_max_f32_e32 v0, v75, v75
	s_waitcnt lgkmcnt(0)
	v_mfma_f32_32x32x16_f16 v[32:47], v[4:7], v[84:87], v[32:47]
	v_cvt_pk_f16_f32 v25, v2, v3
	v_max_f32_e32 v15, 0, v0
	v_max_f32_e32 v0, v76, v76
	v_max_f32_e32 v1, v77, v77
	v_max_f32_e32 v2, v78, v78
	v_max_f32_e32 v3, v79, v79
	v_max_f32_e32 v0, 0, v0
	v_max_f32_e32 v1, 0, v1
	v_max_f32_e32 v2, 0, v2
	v_max_f32_e32 v3, 0, v3
	v_cvt_pk_f16_f32 v31, v2, v3
	v_cvt_pk_f16_f32 v30, v0, v1
	ds_read_b128 v[0:3], v93 offset:640
	ds_read_b128 v[8:11], v94 offset:21504
	v_max_f32_e32 v4, v48, v48
	v_cvt_pk_f16_f32 v28, v12, v13
	v_max_f32_e32 v12, 0, v4
	v_max_f32_e32 v4, v49, v49
	v_max_f32_e32 v13, 0, v4
	ds_read_b128 v[4:7], v94 offset:22528
	s_waitcnt lgkmcnt(1)
	v_mfma_f32_32x32x16_f16 v[32:47], v[8:11], v[88:91], v[32:47]
	v_max_f32_e32 v8, v50, v50
	v_cvt_pk_f16_f32 v29, v14, v15
	v_max_f32_e32 v14, 0, v8
	v_max_f32_e32 v8, v51, v51
	v_max_f32_e32 v15, 0, v8
	v_max_f32_e32 v8, v52, v52
	v_max_f32_e32 v48, 0, v8
	ds_read_b128 v[8:11], v94 offset:23552
	s_waitcnt lgkmcnt(1)
	v_mfma_f32_32x32x16_f16 v[32:47], v[4:7], v[16:19], v[32:47]
	v_max_f32_e32 v4, v53, v53
	v_max_f32_e32 v49, 0, v4
	v_max_f32_e32 v4, v54, v54
	v_max_f32_e32 v50, 0, v4
	v_max_f32_e32 v4, v55, v55
	v_max_f32_e32 v51, 0, v4
	ds_read_b128 v[4:7], v94 offset:24576
	s_waitcnt lgkmcnt(1)
	v_mfma_f32_32x32x16_f16 v[32:47], v[8:11], v[20:23], v[32:47]
	v_max_f32_e32 v8, v56, v56
	v_cvt_pk_f16_f32 v51, v50, v51
	v_cvt_pk_f16_f32 v50, v48, v49
	v_cvt_pk_f16_f32 v48, v12, v13
	v_max_f32_e32 v12, 0, v8
	ds_read_b128 v[8:11], v94 offset:25600
	v_cvt_pk_f16_f32 v49, v14, v15
	s_waitcnt lgkmcnt(1)
	v_mfma_f32_32x32x16_f16 v[32:47], v[4:7], v[24:27], v[32:47]
	v_max_f32_e32 v4, v57, v57
	v_max_f32_e32 v13, 0, v4
	v_max_f32_e32 v4, v58, v58
	v_max_f32_e32 v14, 0, v4
	v_max_f32_e32 v4, v59, v59
	v_max_f32_e32 v15, 0, v4
	ds_read_b128 v[4:7], v94 offset:26624
	s_waitcnt lgkmcnt(1)
	v_mfma_f32_32x32x16_f16 v[32:47], v[8:11], v[28:31], v[32:47]
	v_max_f32_e32 v8, v60, v60
	v_max_f32_e32 v52, 0, v8
	v_max_f32_e32 v8, v61, v61
	v_max_f32_e32 v53, 0, v8
	v_max_f32_e32 v8, v62, v62
	v_max_f32_e32 v54, 0, v8
	ds_read_b128 v[8:11], v94 offset:27648
	s_waitcnt lgkmcnt(1)
	v_mfma_f32_32x32x16_f16 v[32:47], v[4:7], v[48:51], v[32:47]
	ds_read_b128 v[56:59], v94 offset:28672
	v_max_f32_e32 v4, v63, v63
	v_max_f32_e32 v4, 0, v4
	v_cvt_pk_f16_f32 v55, v54, v4
	v_cvt_pk_f16_f32 v54, v52, v53
	v_cvt_pk_f16_f32 v53, v14, v15
	v_cvt_pk_f16_f32 v52, v12, v13
	s_waitcnt lgkmcnt(1)
	s_nop 0
	v_mfma_f32_32x32x16_f16 v[32:47], v[8:11], v[52:55], v[32:47]
	ds_read_b128 v[4:7], v93 offset:672
	ds_read_b128 v[8:11], v93 offset:704
	ds_read_b128 v[12:15], v93 offset:736
	ds_read_b128 v[60:63], v94 offset:29696
	ds_read_b128 v[64:67], v93 offset:768
	s_waitcnt lgkmcnt(2)
	v_mfma_f32_32x32x16_f16 v[0:15], v[56:59], v[84:87], v[0:15]
	s_waitcnt lgkmcnt(1)
	v_mfma_f32_32x32x16_f16 v[0:15], v[60:63], v[88:91], v[0:15]
	ds_read_b128 v[56:59], v94 offset:30720
	ds_read_b128 v[60:63], v94 offset:31744
	s_waitcnt lgkmcnt(1)
	v_mfma_f32_32x32x16_f16 v[0:15], v[56:59], v[16:19], v[0:15]
	s_waitcnt lgkmcnt(0)
	v_mfma_f32_32x32x16_f16 v[0:15], v[60:63], v[20:23], v[0:15]
	ds_read_b128 v[16:19], v94 offset:32768
	ds_read_b128 v[20:23], v94 offset:33792
	s_waitcnt lgkmcnt(1)
	v_mfma_f32_32x32x16_f16 v[0:15], v[16:19], v[24:27], v[0:15]
	s_waitcnt lgkmcnt(0)
	v_mfma_f32_32x32x16_f16 v[0:15], v[20:23], v[28:31], v[0:15]
	ds_read_b128 v[16:19], v94 offset:34816
	ds_read_b128 v[20:23], v94 offset:35840
	s_waitcnt lgkmcnt(1)
	v_mfma_f32_32x32x16_f16 v[0:15], v[16:19], v[48:51], v[0:15]
	v_max_f32_e32 v16, v32, v32
	v_max_f32_e32 v16, 0, v16
	v_max_f32_e32 v17, v33, v33
	v_fma_f32 v16, v64, v16, 0
	v_max_f32_e32 v17, 0, v17
	v_fmac_f32_e32 v16, v65, v17
	v_max_f32_e32 v17, v34, v34
	s_waitcnt lgkmcnt(0)
	v_mfma_f32_32x32x16_f16 v[0:15], v[20:23], v[52:55], v[0:15]
	v_max_f32_e32 v17, 0, v17
	ds_read_b128 v[18:21], v93 offset:800
	ds_read_b128 v[22:25], v93 offset:832
	v_fmac_f32_e32 v16, v66, v17
	v_max_f32_e32 v17, v35, v35
	v_max_f32_e32 v17, 0, v17
	v_fmac_f32_e32 v16, v67, v17
	v_max_f32_e32 v17, v36, v36
	v_max_f32_e32 v17, 0, v17
	s_waitcnt lgkmcnt(1)
	v_fmac_f32_e32 v16, v18, v17
	v_max_f32_e32 v17, v37, v37
	v_max_f32_e32 v17, 0, v17
	v_fmac_f32_e32 v16, v19, v17
	v_max_f32_e32 v17, v38, v38
	v_max_f32_e32 v17, 0, v17
	v_fmac_f32_e32 v16, v20, v17
	v_max_f32_e32 v17, v39, v39
	v_max_f32_e32 v17, 0, v17
	v_fmac_f32_e32 v16, v21, v17
	v_max_f32_e32 v17, v40, v40
	v_max_f32_e32 v17, 0, v17
	s_waitcnt lgkmcnt(0)
	v_fmac_f32_e32 v16, v22, v17
	v_max_f32_e32 v17, v41, v41
	v_max_f32_e32 v17, 0, v17
	v_fmac_f32_e32 v16, v23, v17
	v_max_f32_e32 v17, v42, v42
	v_max_f32_e32 v17, 0, v17
	ds_read_b128 v[18:21], v93 offset:864
	v_fmac_f32_e32 v16, v24, v17
	v_max_f32_e32 v17, v43, v43
	v_max_f32_e32 v17, 0, v17
	v_fmac_f32_e32 v16, v25, v17
	v_max_f32_e32 v17, v44, v44
	v_max_f32_e32 v17, 0, v17
	ds_read_b128 v[22:25], v93 offset:896
	s_waitcnt lgkmcnt(1)
	v_fmac_f32_e32 v16, v18, v17
	v_max_f32_e32 v17, v45, v45
	v_max_f32_e32 v17, 0, v17
	v_fmac_f32_e32 v16, v19, v17
	v_max_f32_e32 v17, v46, v46
	v_max_f32_e32 v17, 0, v17
	v_fmac_f32_e32 v16, v20, v17
	v_max_f32_e32 v17, v47, v47
	v_max_f32_e32 v17, 0, v17
	v_max_f32_e32 v0, v0, v0
	v_fmac_f32_e32 v16, v21, v17
	v_max_f32_e32 v0, 0, v0
	s_waitcnt lgkmcnt(0)
	v_fmac_f32_e32 v16, v22, v0
	v_max_f32_e32 v0, v1, v1
	v_max_f32_e32 v0, 0, v0
	v_fmac_f32_e32 v16, v23, v0
	v_max_f32_e32 v0, v2, v2
	v_max_f32_e32 v0, 0, v0
	v_fmac_f32_e32 v16, v24, v0
	v_max_f32_e32 v0, v3, v3
	v_max_f32_e32 v17, 0, v0
	ds_read_b128 v[0:3], v93 offset:928
	ds_read_b128 v[18:21], v93 offset:960
	v_max_f32_e32 v4, v4, v4
	v_fmac_f32_e32 v16, v25, v17
	v_max_f32_e32 v4, 0, v4
	s_waitcnt lgkmcnt(1)
	v_fmac_f32_e32 v16, v0, v4
	v_max_f32_e32 v0, v5, v5
	v_max_f32_e32 v0, 0, v0
	v_fmac_f32_e32 v16, v1, v0
	v_max_f32_e32 v0, v6, v6
	v_max_f32_e32 v0, 0, v0
	v_fmac_f32_e32 v16, v2, v0
	v_max_f32_e32 v0, v7, v7
	v_max_f32_e32 v0, 0, v0
	v_fmac_f32_e32 v16, v3, v0
	v_max_f32_e32 v0, v8, v8
	v_max_f32_e32 v0, 0, v0
	s_waitcnt lgkmcnt(0)
	v_fmac_f32_e32 v16, v18, v0
	v_max_f32_e32 v0, v9, v9
	v_max_f32_e32 v0, 0, v0
	v_fmac_f32_e32 v16, v19, v0
	v_max_f32_e32 v0, v10, v10
	v_max_f32_e32 v0, 0, v0
	v_fmac_f32_e32 v16, v20, v0
	v_max_f32_e32 v0, v11, v11
	v_max_f32_e32 v0, 0, v0
	v_fmac_f32_e32 v16, v21, v0
	v_max_f32_e32 v0, v12, v12
	v_max_f32_e32 v0, 0, v0
	v_fmac_f32_e32 v16, v80, v0
	v_max_f32_e32 v0, v13, v13
	v_max_f32_e32 v0, 0, v0
	v_fmac_f32_e32 v16, v81, v0
	v_max_f32_e32 v0, v14, v14
	v_max_f32_e32 v0, 0, v0
	v_fmac_f32_e32 v16, v82, v0
	v_max_f32_e32 v0, v15, v15
	v_max_f32_e32 v0, 0, v0
	v_fmac_f32_e32 v16, v83, v0
	v_mov_b32_e32 v0, v16
	s_nop 1
	v_permlane32_swap_b32_e32 v16, v0
	s_and_saveexec_b64 s[0:1], vcc
	s_cbranch_execz .LBB0_123
	s_mov_b32 s0, s88
	v_add_f32_e32 v0, v16, v0
	s_waitcnt lgkmcnt(0)
	v_add_f32_e32 v0, s0, v0
	v_mul_f32_e32 v0, 0xbfb8aa3b, v0
	v_exp_f32_e32 v1, v0
	s_or_b32 s0, s31, s30
	v_or_b32_e32 v0, s0, v92
	v_add_f32_e32 v2, 1.0, v1
	v_div_scale_f32 v3, s[0:1], v2, v2, 1.0
	v_rcp_f32_e32 v4, v3
	v_div_scale_f32 v5, vcc, 1.0, v2, 1.0
	v_ashrrev_i32_e32 v1, 31, v0
	v_fma_f32 v6, -v3, v4, 1.0
	v_fmac_f32_e32 v4, v6, v4
	v_mul_f32_e32 v6, v5, v4
	v_fma_f32 v7, -v3, v6, v5
	v_fmac_f32_e32 v6, v7, v4
	v_fma_f32 v3, -v3, v6, v5
	v_div_fmas_f32 v3, v3, v4, v6
	v_div_fixup_f32 v2, v3, v2, 1.0
	v_lshl_add_u64 v[0:1], v[0:1], 2, s[22:23]
	global_store_dword v[0:1], v2, off sc0 sc1
